# sliding-window unit loop: key positions of the prefetched tile no longer waited for right behind the prefetch loads (raw positions kept in a register, converted one step later)
# baseline (speedup 1.0000x reference)
;     ...
;     {   const bool h1 = DESC ? (t > 0) : (t < t_hi); const int t1 = DESC ? t - 1 : t + 1;
;         AT_LOAD(t); AT_STORE(0);
;         if (h1) AT_LOAD(t1);
;         __syncthreads(); }
.LBB0_1032:
	s_or_b64 exec, exec, s[46:47]
	s_movk_i32 s28, 0x90
	v_mul_lo_u32 v148, v8, s28
	v_lshlrev_b32_e32 v151, 4, v11
	v_add_u32_e32 v11, v148, v151
	v_mul_lo_u32 v159, v9, s28
	v_lshlrev_b32_e32 v160, 4, v12
	s_waitcnt vmcnt(3)
	ds_write_b128 v11, v[96:99]
	v_add_u32_e32 v11, v159, v160
	s_movk_i32 s28, 0xc0
	s_waitcnt vmcnt(2)
	ds_write_b128 v11, v[100:103]
	v_mul_lo_u32 v11, v117, s28
	v_lshl_add_u32 v161, v10, 4, v11
	v_mov_b32_e32 v10, 0x15000
	s_movk_i32 s48, 0x90
	v_lshl_add_u32 v162, v118, 2, v10
	s_waitcnt vmcnt(1)
	ds_write_b128 v161, v[104:107] offset:36864
	s_waitcnt vmcnt(0)
	ds_write_b128 v161, v[108:111] offset:49152
	s_and_saveexec_b64 s[46:47], s[40:41]
	ds_write_b32 v162, v158
	s_or_b64 exec, exec, s[46:47]
	s_lshr_b32 s3, s3, 7
	s_ashr_i32 s20, s20, 3
	s_cmp_ge_i32 s3, s20
	s_cbranch_scc1 .LBB0_1038
	s_add_i32 s45, s44, 0x80
	v_add_u32_e32 v12, s45, v8
	v_mov_b64_e32 v[10:11], s[42:43]
	v_mad_i64_i32 v[12:13], s[28:29], v12, s33, v[10:11]
	v_add_u32_e32 v14, s45, v9
	v_lshl_add_u64 v[12:13], v[0:1], 1, v[12:13]
	v_mad_i64_i32 v[10:11], s[28:29], v14, s33, v[10:11]
	v_lshl_add_u64 v[10:11], v[2:3], 1, v[10:11]
	global_load_dwordx4 v[96:99], v[12:13], off offset:3392
	global_load_dwordx4 v[100:103], v[10:11], off offset:3392
	v_add_u32_e32 v12, s45, v117
	v_mad_i64_i32 v[10:11], s[28:29], v12, s33, v[120:121]
	v_add_u32_e32 v12, 64, v12
	v_mad_i64_i32 v[12:13], s[28:29], v12, s33, v[120:121]
	global_load_dwordx4 v[104:107], v[10:11], off offset:3648
	global_load_dwordx4 v[108:111], v[12:13], off offset:3648
	s_and_saveexec_b64 s[46:47], s[40:41]
	s_cbranch_execz .LBB0_1037
	s_ashr_i32 s45, s44, 31
	v_lshl_add_u64 v[10:11], v[118:119], 0, s[44:45]
	v_lshl_add_u64 v[10:11], v[10:11], 2, s[6:7]
	global_load_dword v193, v[10:11], off offset:512

; #define LAS __attribute__((address_space(3)))
; #define AT_SUB(sub_, pm_) do { bool want_; AT_WANT(2 * t + (sub_), pm_, want_); \
;         if (want_) { AT_QK(st, t * 128 + (sub_) * 64, b0 * KB2 + (sub_) * 64 * KS, BBASE + b0 * 512 + (sub_) * 256); AT_SMPV(st, VBASE + b0 * VB2 + (sub_) * 64 * VS); } } while (0)
;     ...
;         const bool has_next = DESC ? (t > 0) : (t < t_hi); const int tn = DESC ? t - 1 : t + 1;
;         const bool has_next2 = has_next && (DESC ? (tn > 0) : (tn < t_hi)); const int tn2 = DESC ? tn - 1 : tn + 1;
;         int pm0 = 0, pm1 = 0; if (DESC) { pm0 = pmaxpre[2 * t]; pm1 = pmaxpre[2 * t + 1]; }
;         if (DESC) { AT_SUB(1, pm1); AT_SUB(0, pm0); } else { AT_SUB(0, pm0); AT_SUB(1, pm1); }
;         if (DESC && lane == 0) *(volatile LAS int*)(lds + FLG + par * 32 + wv * 4) = fin ? 1 : 0;
;         if (has_next) AT_STORE(b1);
;         if (has_next2) AT_LOAD(tn2);
.LBB0_1055:
	s_cmp_lt_i32 s3, s20
	s_cselect_b64 s[44:45], -1, 0
	s_cmp_ge_i32 s3, s20
	s_cselect_b64 s[42:43], -1, 0
	s_and_b64 vcc, exec, s[42:43]
	s_cbranch_vccnz .LBB0_1059
	s_mul_i32 s46, s95, 0x4800
	v_add3_u32 v0, s46, v148, v151
	s_waitcnt vmcnt(3)
	ds_write_b128 v0, v[96:99]
	v_add3_u32 v0, s46, v159, v160
	s_mul_i32 s46, s95, 0x6000
	s_waitcnt vmcnt(2)
	ds_write_b128 v0, v[100:103]
	v_add_u32_e32 v0, s46, v161
	s_waitcnt vmcnt(1)
	ds_write_b128 v0, v[104:107] offset:36864
	s_waitcnt vmcnt(0)
	ds_write_b128 v0, v[108:111] offset:49152
	s_and_saveexec_b64 s[46:47], s[40:41]
	v_sub_u32_e32 v158, v193, v115
	v_cvt_f32_i32_e32 v158, v158
	v_lshl_add_u32 v0, s95, 9, v162
	ds_write_b32 v0, v158
	s_or_b64 exec, exec, s[46:47]
.LBB0_1059:
	s_add_i32 s3, s3, 1
	s_cmp_lt_i32 s3, s20
	s_cselect_b64 s[46:47], -1, 0
	s_and_b64 s[44:45], s[44:45], s[46:47]
	s_andn2_b64 vcc, exec, s[44:45]
	s_cbranch_vccnz .LBB0_1063
	v_add_u32_e32 v0, s93, v171
	v_add_u32_e32 v2, s93, v170
	v_mad_i64_i32 v[0:1], s[44:45], v0, s33, v[124:125]
	v_mad_i64_i32 v[2:3], s[44:45], v2, s33, v[126:127]
	global_load_dwordx4 v[96:99], v[0:1], off offset:3392
	global_load_dwordx4 v[100:103], v[2:3], off offset:3392
	v_add_u32_e32 v2, s93, v117
	v_add_u32_e32 v0, 0x100, v2
	v_mad_i64_i32 v[0:1], s[44:45], v0, s33, v[120:121]
	v_add_u32_e32 v2, 0x140, v2
	v_mad_i64_i32 v[2:3], s[44:45], v2, s33, v[120:121]
	global_load_dwordx4 v[104:107], v[0:1], off offset:3648
	global_load_dwordx4 v[108:111], v[2:3], off offset:3648
	s_and_saveexec_b64 s[44:45], s[40:41]
	s_cbranch_execz .LBB0_1062
	v_add_u32_e32 v0, s93, v169
	v_ashrrev_i32_e32 v1, 31, v0
	v_lshl_add_u64 v[0:1], v[0:1], 2, s[6:7]
	global_load_dword v193, v[0:1], off
